# sel tile head: scalar block-id extraction used as the cmp-to-cndmask filler, K reads as the mov-to-MFMA filler, s_nop pads gone
# speedup vs baseline: 1.0445x; 1.0011x over previous
; __device__ __forceinline__ unsigned lds_addr(const LAS void* p) { return (unsigned)(size_t)p; }
; template <bool DUMMY> __device__ __forceinline__ void sel_phase(Frame& F) {
;     ...
;                 const unsigned a0 = byte & 0xfu, a1 = byte >> 4;
;                 if (byte == 0u) continue;
;                 const bool selA = ((a0 >> (c >> 2)) & 1u) != 0u, selB = ((a1 >> (c >> 2)) & 1u) != 0u;
;                 const float NINF = -__builtin_inff();
;                 const int kb = jc * 64; const bool diag = (jc == cur); f32x4 s0[4], s1[4];
;                 const float bA = selA ? 0.f : NINF, bB = selB ? 0.f : NINF;
;                 if (a0 != 0u) {
;                     const float rf = sm8_ref(g0);
;                     VT8Frag vf; qk8_tile_c(s0, g0, lds_addr(sb) + (unsigned)klane, bA + (5.f - rf)); pv8_issue(vf, lds_addr(sb + K8TB) + (unsigned)vtlane);
;                     if (diag) mask_scores(s0, tokA, 0x40000000u, kb, kq);
.Lsel_nodma:
	s_lshr_b32 s45, s67, s36
	s_and_b32 s97, s45, 0xff
	s_cbranch_scc0 .LBB0_1798
	ds_read_b128 v[84:87], v208 offset:0
	ds_read_b128 v[88:91], v208 offset:16
	ds_read_b128 v[92:95], v208 offset:0x900
	ds_read_b128 v[96:99], v208 offset:0x910
	ds_read_b128 v[118:121], v208 offset:0x1200
	ds_read_b128 v[122:125], v208 offset:0x1210
	s_and_b32 vcc_lo, s45, 15
	s_cbranch_scc0 .Lsel_g1_pre
	v_and_b32_e32 v18, s45, v154
	v_cmp_eq_u32_e32 vcc, 0, v18
	s_lshr_b32 s44, s66, s36
	s_and_b32 s44, s44, 0xff
	v_cndmask_b32_e32 v210, v216, v181, vcc
	v_mov_b32_e32 v211, v210
	v_mov_b32_e32 v212, v210
	v_mov_b32_e32 v213, v210
	ds_read_b128 v[126:129], v208 offset:0x1b00
	ds_read_b128 v[130:133], v208 offset:0x1b10
	s_waitcnt lgkmcnt(6)
	v_mfma_scale_f32_16x16x128_f8f6f4 v[84:87], v[84:91], v[0:7], v[210:213], v178, v177 op_sel_hi:[0,0,0]
	ds_read_b64 v[148:149], v207 offset:0
	ds_read_b64 v[146:147], v207 offset:32
	ds_read_b64 v[144:145], v207 offset:0x500
	ds_read_b64 v[142:143], v207 offset:0x520
	ds_read_b64 v[140:141], v207 offset:0xa00
	ds_read_b64 v[136:137], v207 offset:0xa20
	ds_read_b64 v[138:139], v207 offset:0xf00
	ds_read_b64 v[134:135], v207 offset:0xf20
	s_waitcnt lgkmcnt(12)
	v_mfma_scale_f32_16x16x128_f8f6f4 v[88:91], v[92:99], v[0:7], v[210:213], v178, v177 op_sel_hi:[0,0,0]
	s_waitcnt lgkmcnt(10)
	v_mfma_scale_f32_16x16x128_f8f6f4 v[92:95], v[118:125], v[0:7], v[210:213], v178, v177 op_sel_hi:[0,0,0]
	s_waitcnt lgkmcnt(8)
	v_mfma_scale_f32_16x16x128_f8f6f4 v[96:99], v[126:133], v[0:7], v[210:213], v178, v177 op_sel_hi:[0,0,0]
	ds_read_b64 v[132:133], v207 offset:0x1400
	ds_read_b64 v[130:131], v207 offset:0x1420
	ds_read_b64 v[128:129], v207 offset:0x1900
	ds_read_b64 v[126:127], v207 offset:0x1920
	ds_read_b64 v[124:125], v207 offset:0x1e00
	ds_read_b64 v[120:121], v207 offset:0x1e20
	ds_read_b64 v[118:119], v207 offset:0x2300
	ds_read_b64 v[122:123], v207 offset:0x2320
	s_cmp_eq_u32 s44, s58
	s_cbranch_scc0 .LBB0_1806
	s_lshl_b32 s12, s44, 6
	v_add_u32_e32 v18, s12, v155
	v_sub_u32_e32 v114, s55, v18
	v_cmp_gt_u32_e32 vcc, 2.0, v114
	v_sub_u32_e32 v114, v18, v16
	s_nop 2
	v_cndmask_b32_e32 v84, v181, v84, vcc
	v_cmp_lt_u32_e32 vcc, s91, v114
	v_sub_u32_e32 v114, v184, v18
	s_nop 0
	v_cndmask_b32_e32 v85, v181, v85, vcc
	v_cmp_gt_u32_e32 vcc, 2.0, v114
	v_sub_u32_e32 v114, v185, v18
	s_nop 0
	v_cndmask_b32_e32 v86, v181, v86, vcc
	v_cmp_gt_u32_e32 vcc, 2.0, v114
	v_sub_u32_e32 v114, s68, v18
	s_nop 0
	v_cndmask_b32_e32 v87, v181, v87, vcc
	v_cmp_gt_u32_e32 vcc, 2.0, v114
	v_sub_u32_e32 v114, v186, v18
	s_nop 0
	v_cndmask_b32_e32 v88, v181, v88, vcc
	v_cmp_gt_u32_e32 vcc, 2.0, v114
	v_sub_u32_e32 v114, v187, v18
	s_nop 0
	v_cndmask_b32_e32 v89, v181, v89, vcc
	v_cmp_gt_u32_e32 vcc, 2.0, v114
	v_sub_u32_e32 v114, v188, v18
	s_nop 0
	v_cndmask_b32_e32 v90, v181, v90, vcc
	v_cmp_gt_u32_e32 vcc, 2.0, v114
	v_sub_u32_e32 v114, s69, v18
	s_nop 0
	v_cndmask_b32_e32 v91, v181, v91, vcc
	v_cmp_gt_u32_e32 vcc, 2.0, v114
	v_sub_u32_e32 v114, v189, v18
	s_nop 0
	v_cndmask_b32_e32 v92, v181, v92, vcc
	v_cmp_gt_u32_e32 vcc, 2.0, v114
	v_sub_u32_e32 v114, v190, v18
	s_nop 0
	v_cndmask_b32_e32 v93, v181, v93, vcc
	v_cmp_gt_u32_e32 vcc, 2.0, v114
	v_sub_u32_e32 v114, v191, v18
	s_nop 0
	v_cndmask_b32_e32 v94, v181, v94, vcc
	v_cmp_gt_u32_e32 vcc, 2.0, v114
	v_sub_u32_e32 v114, s70, v18
	s_nop 0
	v_cndmask_b32_e32 v95, v181, v95, vcc
	v_cmp_gt_u32_e32 vcc, 2.0, v114
	v_sub_u32_e32 v114, v192, v18
	s_nop 0
	v_cndmask_b32_e32 v96, v181, v96, vcc
	v_cmp_gt_u32_e32 vcc, 2.0, v114
	v_sub_u32_e32 v114, v193, v18
	v_sub_u32_e32 v18, v194, v18
	v_cndmask_b32_e32 v97, v181, v97, vcc
	v_cmp_gt_u32_e32 vcc, 2.0, v114
	s_nop 1
	v_cndmask_b32_e32 v98, v181, v98, vcc
	v_cmp_gt_u32_e32 vcc, 2.0, v18
	s_nop 1
	v_cndmask_b32_e32 v99, v181, v99, vcc

; __device__ __forceinline__ unsigned lds_addr(const LAS void* p) { return (unsigned)(size_t)p; }
; template <bool DUMMY> __device__ __forceinline__ void sel_phase(Frame& F) {
;     ...
;                 if (a1 != 0u) {
;                     const float rf = sm8_ref(g1);
;                     VT8Frag vf; qk8_tile_c(s0, g1, lds_addr(sb) + (unsigned)klane, bB + (5.f - rf)); pv8_issue(vf, lds_addr(sb + K8TB) + (unsigned)vtlane);
;                     if (diag) mask_scores(s0, tokA + 4, 0x40000000u, kb, kq);
.Lsel_g1_pre:
	s_lshr_b32 s45, s45, 4
	v_and_b32_e32 v18, s45, v154
	v_cmp_eq_u32_e32 vcc, 0, v18
	s_lshr_b32 s44, s66, s36
	s_and_b32 s44, s44, 0xff
	v_cndmask_b32_e32 v210, v220, v181, vcc
	v_mov_b32_e32 v211, v210
	v_mov_b32_e32 v212, v210
	v_mov_b32_e32 v213, v210
	ds_read_b128 v[126:129], v208 offset:0x1b00
	ds_read_b128 v[130:133], v208 offset:0x1b10
	s_waitcnt lgkmcnt(6)
	v_mfma_scale_f32_16x16x128_f8f6f4 v[84:87], v[84:91], v[8:15], v[210:213], v178, v177 op_sel_hi:[0,0,0]
	ds_read_b64 v[148:149], v207 offset:0
	ds_read_b64 v[146:147], v207 offset:32
	ds_read_b64 v[144:145], v207 offset:0x500
	ds_read_b64 v[142:143], v207 offset:0x520
	ds_read_b64 v[140:141], v207 offset:0xa00
	ds_read_b64 v[136:137], v207 offset:0xa20
	ds_read_b64 v[138:139], v207 offset:0xf00
	ds_read_b64 v[134:135], v207 offset:0xf20
	s_waitcnt lgkmcnt(12)
	v_mfma_scale_f32_16x16x128_f8f6f4 v[88:91], v[92:99], v[8:15], v[210:213], v178, v177 op_sel_hi:[0,0,0]
	s_waitcnt lgkmcnt(10)
	v_mfma_scale_f32_16x16x128_f8f6f4 v[92:95], v[118:125], v[8:15], v[210:213], v178, v177 op_sel_hi:[0,0,0]
	s_waitcnt lgkmcnt(8)
	v_mfma_scale_f32_16x16x128_f8f6f4 v[96:99], v[126:133], v[8:15], v[210:213], v178, v177 op_sel_hi:[0,0,0]
	ds_read_b64 v[132:133], v207 offset:0x1400
	ds_read_b64 v[130:131], v207 offset:0x1420
	ds_read_b64 v[128:129], v207 offset:0x1900
	ds_read_b64 v[126:127], v207 offset:0x1920
	ds_read_b64 v[124:125], v207 offset:0x1e00
	ds_read_b64 v[120:121], v207 offset:0x1e20
	ds_read_b64 v[118:119], v207 offset:0x2300
	ds_read_b64 v[122:123], v207 offset:0x2320
	s_cmp_eq_u32 s44, s58
	s_cbranch_scc0 .LBB0_1812
	s_lshl_b32 s12, s44, 6
	v_add_u32_e32 v114, s12, v155
	v_sub_u32_e32 v116, v195, v114
	v_cmp_gt_u32_e32 vcc, 2.0, v116
	v_sub_u32_e32 v116, v114, v195
	s_nop 2
	v_cndmask_b32_e32 v84, v181, v84, vcc
	v_cmp_lt_u32_e32 vcc, s91, v116
	v_sub_u32_e32 v116, v196, v114
	s_nop 0
	v_cndmask_b32_e32 v85, v181, v85, vcc
	v_cmp_gt_u32_e32 vcc, 2.0, v116
	v_sub_u32_e32 v116, v197, v114
	s_nop 0
	v_cndmask_b32_e32 v86, v181, v86, vcc
	v_cmp_gt_u32_e32 vcc, 2.0, v116
	v_sub_u32_e32 v116, s71, v114
	s_nop 0
	v_cndmask_b32_e32 v87, v181, v87, vcc
	v_cmp_gt_u32_e32 vcc, 2.0, v116
	v_sub_u32_e32 v116, v198, v114
	s_nop 0
	v_cndmask_b32_e32 v88, v181, v88, vcc
	v_cmp_gt_u32_e32 vcc, 2.0, v116
	v_sub_u32_e32 v116, v199, v114
	s_nop 0
	v_cndmask_b32_e32 v89, v181, v89, vcc
	v_cmp_gt_u32_e32 vcc, 2.0, v116
	v_sub_u32_e32 v116, v200, v114
	s_nop 0
	v_cndmask_b32_e32 v90, v181, v90, vcc
	v_cmp_gt_u32_e32 vcc, 2.0, v116
	v_sub_u32_e32 v116, s72, v114
	s_nop 0
	v_cndmask_b32_e32 v91, v181, v91, vcc
	v_cmp_gt_u32_e32 vcc, 2.0, v116
	v_sub_u32_e32 v116, v201, v114
	s_nop 0
	v_cndmask_b32_e32 v92, v181, v92, vcc
	v_cmp_gt_u32_e32 vcc, 2.0, v116
	v_sub_u32_e32 v116, v202, v114
	s_nop 0
	v_cndmask_b32_e32 v93, v181, v93, vcc
	v_cmp_gt_u32_e32 vcc, 2.0, v116
	v_sub_u32_e32 v116, v203, v114
	s_nop 0
	v_cndmask_b32_e32 v94, v181, v94, vcc
	v_cmp_gt_u32_e32 vcc, 2.0, v116
	v_sub_u32_e32 v116, s73, v114
	s_nop 0
	v_cndmask_b32_e32 v95, v181, v95, vcc
	v_cmp_gt_u32_e32 vcc, 2.0, v116
	v_sub_u32_e32 v116, v204, v114
	s_nop 0
	v_cndmask_b32_e32 v96, v181, v96, vcc
	v_cmp_gt_u32_e32 vcc, 2.0, v116
	v_sub_u32_e32 v116, v205, v114
	v_sub_u32_e32 v114, v206, v114
	v_cndmask_b32_e32 v97, v181, v97, vcc
	v_cmp_gt_u32_e32 vcc, 2.0, v116
	s_nop 1
	v_cndmask_b32_e32 v98, v181, v98, vcc
	v_cmp_gt_u32_e32 vcc, 2.0, v114
	s_nop 1
	v_cndmask_b32_e32 v99, v181, v99, vcc
